# P12: nt cache policy on the gathered activation (A operand) LDS-DMA loads of the up GEMM, on top of previous best
# speedup vs baseline: 1.1137x; 1.1137x over previous
; #define PG8_STAGE(bufoff, gbase, voff) do { _Pragma("unroll") for (int _i = 0; _i < 2; ++_i) \
;         __builtin_amdgcn_global_load_lds((const unsigned*)((const char*)(gbase) + (voff)[_i]), (PG8_LAS unsigned*)(lds + (bufoff) + ldsw + _i * 8192), 16, 0, 0); } while (0)
;     __device__ __forceinline__ bool next(int i, Unit& u) const { const int L = i * G + c; if (L >= NB * nN) return false; u.z = L / nN; u.pn = L % nN; u.pm = i; return true; }
; template <class Epi, class Sched, bool ALIGN_EPI = false, bool SP2 = false>
; __device__ __forceinline__ void gemm_phase(PG8_LAS unsigned char* lds, const Geo geo, const Sched& S, const Epi& E, const int wave_) {
;     ...
;     for (int i = 0; i < 2; ++i) { int R, C; stage_rc(tid * 16 + i * 8192, R, C); const int Rb = Epi::PERM ? ((R & ~31) + perm32(R & 31)) : R;
;         voffA[i] = (unsigned)(R * geo.lda + C * 2); voffB[i] = (unsigned)(Rb * geo.ldb + C * 2); }
;     unsigned c0[2], c1[2], n0[2], n1[2];
; #pragma unroll
;     for (int i = 0; i < 2; ++i) { c0[i] = voffA[i]; c1[i] = voffA[i]; n0[i] = voffA[i]; n1[i] = voffA[i]; }
;     const size_t kstep = (size_t)(BK * 2);
;     const size_t hstepA = (size_t)geo.hstepA, hstepB = (size_t)geo.hstepB;
;     const unsigned ldsw = (unsigned)wid * 1024u;
;     const int aoff = lds_byte(wr * 64 + fr, fq * 8), boff = lds_byte(wc * 32 + fr, fq * 8);
;     ...
;     Unit cur, nxt; int ui = 0;
;     if (!S.next(0, cur)) return;
;     f32x4 acc[2][2][4][2];
; #pragma unroll
;     for (int a = 0; a < 2; ++a)
; #pragma unroll
;         for (int b = 0; b < 2; ++b)
; #pragma unroll
;             for (int m = 0; m < 4; ++m)
; #pragma unroll
;                 for (int n = 0; n < 2; ++n) acc[a][b][m][n] = (f32x4){0.f, 0.f, 0.f, 0.f};
;     bf16x8 At[4][2], B0[2][2], B1[2][2];
;     i32x8 At8[4], B08[2], B18[2];
;     const char* cA; const char* cB; S.ptrs(cur, cA, cB);
;     S.a_ready(cur);
;     if constexpr (Sched::GATHER) {
; #pragma unroll
;         for (int i = 0; i < 2; ++i) { int R, C; stage_rc(tid * 16 + i * 8192, R, C); c0[i] = S.row_off(0, R) + (unsigned)(C * 2); c1[i] = S.row_off(0, 128 + R) + (unsigned)(C * 2); n0[i] = c0[i]; n1[i] = c1[i]; } }
;     static_assert(SP2, "only the two-super-phase loop is kept in this file");
;     PG8_STAGE(PG8_SB(0, 0), cB, voffB); PG8_STAGE(PG8_SB(0, 1), cB + hstepB, voffB); PG8_STAGE(PG8_SA(0, 0), cA, c0); PG8_STAGE(PG8_SA(0, 1), cA + hstepA, c1);
.LBB0_1515:
	v_bfe_i32 v2, v4, 27, 1
	v_lshlrev_b32_e32 v0, 4, v4
	v_lshrrev_b32_e32 v2, 22, v2
	v_add_u32_e32 v2, v0, v2
	v_and_b32_e32 v2, 0xfffffc00, v2
	v_sub_u32_e32 v2, v0, v2
	v_ashrrev_i32_e32 v1, 31, v4
	v_lshrrev_b32_e32 v3, 4, v2
	v_lshrrev_b32_e32 v1, 26, v1
	v_bitop3_b32 v2, v3, v2, 32 bitop3:0x6c
	v_add_u32_e32 v1, v4, v1
	v_ashrrev_i32_e32 v5, 31, v2
	v_ashrrev_i32_e32 v1, 6, v1
	v_lshrrev_b32_e32 v5, 26, v5
	v_lshlrev_b32_e32 v3, 3, v1
	v_add_u32_e32 v5, v2, v5
	v_and_b32_e32 v3, -16, v3
	v_ashrrev_i32_e32 v6, 6, v5
	v_add_u32_e32 v214, v6, v3
	v_and_b32_e32 v3, 0xc0, v5
	v_sub_u32_e32 v2, v2, v3
	v_mov_b32_e32 v3, 1
	v_lshlrev_b32_e32 v1, 5, v1
	v_ashrrev_i16_sdwa v2, v3, sext(v2) dst_sel:DWORD dst_unused:UNUSED_PAD src0_sel:DWORD src1_sel:BYTE_0
	v_and_b32_e32 v1, 32, v1
	v_bfe_i32 v2, v2, 0, 16
	v_add_u32_e32 v0, 0x2000, v0
	v_add_lshl_u32 v215, v1, v2, 1
	v_ashrrev_i32_e32 v1, 31, v0
	v_lshrrev_b32_e32 v1, 22, v1
	v_add_u32_e32 v1, v0, v1
	v_ashrrev_i32_e32 v1, 10, v1
	v_mul_i32_i24_e32 v2, 0x400, v1
	v_lshlrev_b32_e32 v5, 1, v214
	v_lshrrev_b32_e32 v7, 2, v214
	v_and_b32_e32 v6, 3, v6
	s_mov_b32 s1, 0x1fffe0
	v_sub_u32_e32 v0, v0, v2
	v_and_b32_e32 v5, 24, v5
	v_and_b32_e32 v7, 4, v7
	v_and_or_b32 v6, v214, s1, v6
	v_lshrrev_b32_e32 v2, 4, v0
	v_or3_b32 v5, v6, v7, v5
	v_bitop3_b32 v0, v2, v0, 32 bitop3:0x6c
	v_lshl_add_u32 v196, v5, 11, v215
	v_ashrrev_i32_e32 v5, 31, v0
	v_lshrrev_b32_e32 v5, 26, v5
	v_lshlrev_b32_e32 v2, 3, v1
	v_add_u32_e32 v5, v0, v5
	v_and_b32_e32 v2, -16, v2
	v_ashrrev_i32_e32 v6, 6, v5
	s_add_u32 s10, s78, 0x67dc8000
	v_add_u32_e32 v216, v6, v2
	v_and_b32_e32 v2, 0xc0, v5
	v_and_b32_e32 v5, 3, v6
	s_addc_u32 s11, s79, 0
	v_sub_u32_e32 v0, v0, v2
	v_and_or_b32 v5, v216, s1, v5
	s_lshl_b32 s1, s38, 2
	v_ashrrev_i16_sdwa v0, v3, sext(v0) dst_sel:DWORD dst_unused:UNUSED_PAD src0_sel:DWORD src1_sel:BYTE_0
	v_lshlrev_b32_e32 v2, 1, v216
	v_lshrrev_b32_e32 v3, 2, v216
	s_add_i32 s1, s1, 0
	v_and_b32_e32 v2, 24, v2
	v_and_b32_e32 v3, 4, v3
	s_add_i32 s1, s1, 0x22c00
	v_or3_b32 v2, v5, v3, v2
	v_mov_b32_e32 v3, s1
	ds_read_b32 v3, v3
	v_lshlrev_b32_e32 v1, 5, v1
	v_and_b32_e32 v1, 32, v1
	v_bfe_i32 v0, v0, 0, 16
	v_add_lshl_u32 v217, v1, v0, 1
	s_waitcnt lgkmcnt(0)
	v_readfirstlane_b32 s6, v3
	s_ashr_i32 s1, s2, 6
	s_ashr_i32 s7, s6, 31
	s_ashr_i32 s41, s40, 31
	s_ashr_i32 s0, s2, 8
	v_lshl_add_u32 v198, v2, 11, v217
	s_lshl_b32 s8, s1, 10
	s_lshl_b64 s[6:7], s[6:7], 23
	v_lshl_add_u32 v0, v214, 2, s4
	v_lshl_add_u32 v2, v216, 2, s4
	s_lshl_b64 s[4:5], s[40:41], 18
	s_add_u32 s6, s88, s6
	s_addc_u32 s7, s87, s7
	s_add_u32 s6, s6, s4
	s_addc_u32 s7, s7, s5
	s_add_i32 s31, s8, 0
	ds_read2st64_b32 v[0:1], v0 offset1:2
	s_add_i32 s41, s31, 0x10000
	s_add_i32 s50, s31, 0x12000
	ds_read2st64_b32 v[2:3], v2 offset1:2
	s_mov_b32 m0, s41
	s_add_u32 s4, s6, 0x400000
	global_load_lds_dwordx4 v196, s[6:7] nt
	s_mov_b32 m0, s50
	s_addc_u32 s5, s7, 0
	s_add_i32 s51, s31, 0x14000
	global_load_lds_dwordx4 v198, s[6:7] nt
	s_mov_b32 m0, s51
	s_add_i32 s52, s31, 0x16000
	global_load_lds_dwordx4 v196, s[4:5] nt
	s_mov_b32 m0, s52
	s_waitcnt lgkmcnt(0)
	v_lshl_add_u32 v64, v0, 11, v215
	global_load_lds_dwordx4 v198, s[4:5] nt
	s_mov_b32 m0, s31
	s_add_i32 s53, s31, 0x2000
	v_lshl_add_u32 v200, v2, 11, v217
	global_load_lds_dwordx4 v64, s[10:11] nt
	s_mov_b32 m0, s53
	s_add_i32 s54, s31, 0x4000
	v_lshl_add_u32 v202, v1, 11, v215
	global_load_lds_dwordx4 v200, s[10:11] nt
	s_mov_b32 m0, s54
	s_add_i32 s55, s31, 0x6000
	v_lshl_add_u32 v204, v3, 11, v217
	global_load_lds_dwordx4 v202, s[10:11] nt
	s_mov_b32 m0, s55
	v_writelane_b32 v254, s94, 63
	global_load_lds_dwordx4 v204, s[10:11] nt
	v_writelane_b32 v254, s89, 60
	v_writelane_b32 v255, s84, 0
	v_writelane_b32 v254, s88, 58
	s_cmp_eq_u32 s0, 1
	v_writelane_b32 v255, s85, 1
	v_writelane_b32 v254, s87, 61
	v_mov_b32_e32 v65, 0
	s_cselect_b64 s[4:5], -1, 0
	v_writelane_b32 v255, s97, 2
	v_mov_b32_e32 v197, v65
	v_mov_b32_e32 v199, v65
	v_writelane_b32 v254, s4, 42
	v_writelane_b32 v255, s96, 3
	s_movk_i32 s56, 0x2000
	s_mov_b32 s65, 0
	s_mov_b32 s57, 0x10000
	v_lshl_add_u64 v[2:3], s[6:7], 0, v[196:197]
	v_lshl_add_u64 v[0:1], s[6:7], 0, v[198:199]
	s_mov_b32 s58, 0x12000
	s_mov_b32 s59, 0x14000
	s_mov_b32 s60, 0x16000
	v_mov_b32_e32 v201, v65
	s_movk_i32 s61, 0x4000
	v_writelane_b32 v254, s5, 43
	s_cmp_lg_u32 s0, 1
	s_movk_i32 s62, 0x6000
	s_cbranch_scc1 .LBB0_1517
	s_barrier

; #define PG8_STAGE(bufoff, gbase, voff) do { _Pragma("unroll") for (int _i = 0; _i < 2; ++_i) \
;         __builtin_amdgcn_global_load_lds((const unsigned*)((const char*)(gbase) + (voff)[_i]), (PG8_LAS unsigned*)(lds + (bufoff) + ldsw + _i * 8192), 16, 0, 0); } while (0)
; #define PG8_WAIT_V(n) asm volatile("s_waitcnt vmcnt(" #n ")" ::: "memory")
; #define PG8_WAIT_L(n) asm volatile("s_waitcnt lgkmcnt(" #n ")" ::: "memory")
; #define PG8_BAR __builtin_amdgcn_s_barrier()
; #define PG8_SCHED __builtin_amdgcn_sched_barrier(0)
; template <class Epi, class Sched, bool ALIGN_EPI = false, bool SP2 = false>
; __device__ __forceinline__ void gemm_phase(PG8_LAS unsigned char* lds, const Geo geo, const Sched& S, const Epi& E, const int wave_) {
;     ...
;             PG8_LDB(B0, 0, 0); PG8_LDB(B1, 0, 1); PG8_SCHED; PG8_LDA(At, 0, 0); PG8_STAGE(PG8_SA(1, 1), a1 + hstepA, c1);
;             PG8_WAIT_V(8); PG8_WAIT_L(0); PG8_BAR; PG8_MMA(0, 0, At, B0); PG8_MMA(0, 1, At, B1); PG8_BAR; PG8_SCHED;
;             PG8_LDA(At, 0, 1); PG8_STAGE(PG8_SB(0, 0), b2, voffB); PG8_STAGE(PG8_SB(0, 1), b2 + hstepB, voffB); PG8_STAGE(PG8_SA(0, 0), a2, s0);
;             PG8_WAIT_V(8); PG8_WAIT_L(0); PG8_BAR; if (h1) { PG8_MMA(1, 0, At, B0); PG8_MMA(1, 1, At, B1); } PG8_BAR; PG8_SCHED;
.LBB0_1528:
	ds_read_b128 v[16:19], v201
	ds_read_b128 v[20:23], v220
	ds_read_b128 v[24:27], v221
	ds_read_b128 v[28:31], v222
	ds_read_b128 v[0:3], v223
	ds_read_b128 v[4:7], v224
	ds_read_b128 v[8:11], v225
	ds_read_b128 v[12:15], v226
	s_add_u32 s8, s78, s44
	s_addc_u32 s9, s79, s45
	s_add_u32 s46, s8, 0x67dc8100
	s_addc_u32 s47, s9, 0
	s_and_b64 s[8:9], s[6:7], exec
	s_cselect_b32 s49, s11, s47
	s_cselect_b32 s48, s10, s46
	s_add_u32 s46, s39, s44
	s_addc_u32 s47, s66, s45
	s_and_b64 s[8:9], s[6:7], exec
	s_cselect_b32 s47, s37, s47
	s_cselect_b32 s46, s36, s46
	v_cndmask_b32_e64 v64, v240, v203, s[6:7]
	v_cndmask_b32_e64 v66, v200, v238, s[6:7]
	v_lshl_add_u64 v[210:211], v[208:209], 0, s[44:45]
	s_add_i32 m0, s31, 0xc000
	s_waitcnt lgkmcnt(0)
	ds_read_b128 v[32:35], v235
	ds_read_b128 v[36:39], v235 offset:1024
	ds_read_b128 v[40:43], v235 offset:2048
	ds_read_b128 v[44:47], v235 offset:3072
	ds_read_b128 v[48:51], v235 offset:4096
	ds_read_b128 v[52:55], v235 offset:5120
	ds_read_b128 v[56:59], v235 offset:6144
	ds_read_b128 v[60:63], v235 offset:7168
	global_load_lds_dwordx4 v[210:211], off
	v_lshl_add_u64 v[210:211], v[206:207], 0, s[44:45]
	s_add_i32 m0, s31, 0xe000
	s_nop 0
	global_load_lds_dwordx4 v[210:211], off
	s_waitcnt vmcnt(8)
	s_waitcnt lgkmcnt(0)
	s_barrier
	s_setprio 1
	s_waitcnt lgkmcnt(0)
	v_mfma_f32_16x16x128_f8f6f4 v[192:195], v[16:23], v[32:39], v[192:195]
	v_mfma_f32_16x16x128_f8f6f4 v[184:187], v[24:31], v[32:39], v[184:187]
	v_mfma_f32_16x16x128_f8f6f4 v[176:179], v[16:23], v[40:47], v[176:179]
	v_mfma_f32_16x16x128_f8f6f4 v[168:171], v[24:31], v[40:47], v[168:171]
	v_mfma_f32_16x16x128_f8f6f4 v[160:163], v[16:23], v[48:55], v[160:163]
	v_mfma_f32_16x16x128_f8f6f4 v[152:155], v[24:31], v[48:55], v[152:155]
	v_mfma_f32_16x16x128_f8f6f4 v[144:147], v[16:23], v[56:63], v[144:147]
	v_mfma_f32_16x16x128_f8f6f4 v[136:139], v[24:31], v[56:63], v[136:139]
	s_setprio 0
	s_setprio 1
	v_mfma_f32_16x16x128_f8f6f4 v[188:191], v[0:7], v[32:39], v[188:191]
	v_mfma_f32_16x16x128_f8f6f4 v[180:183], v[8:15], v[32:39], v[180:183]
	v_mfma_f32_16x16x128_f8f6f4 v[172:175], v[0:7], v[40:47], v[172:175]
	v_mfma_f32_16x16x128_f8f6f4 v[164:167], v[8:15], v[40:47], v[164:167]
	v_mfma_f32_16x16x128_f8f6f4 v[156:159], v[0:7], v[48:55], v[156:159]
	v_mfma_f32_16x16x128_f8f6f4 v[148:151], v[8:15], v[48:55], v[148:151]
	v_mfma_f32_16x16x128_f8f6f4 v[140:143], v[0:7], v[56:63], v[140:143]
	v_mfma_f32_16x16x128_f8f6f4 v[132:135], v[8:15], v[56:63], v[132:135]
	s_setprio 0
	s_barrier
	s_mov_b32 m0, s41
	v_lshl_add_u64 v[210:211], s[46:47], 0, v[196:197]
	s_add_u32 s8, s46, 0x400000
	ds_read_b128 v[56:59], v235 offset:16384
	ds_read_b128 v[60:63], v235 offset:17408
	ds_read_b128 v[48:51], v235 offset:18432
	ds_read_b128 v[52:55], v235 offset:19456
	ds_read_b128 v[40:43], v235 offset:20480
	ds_read_b128 v[44:47], v235 offset:21504
	ds_read_b128 v[32:35], v235 offset:22528
	ds_read_b128 v[36:39], v235 offset:23552
	global_load_lds_dwordx4 v[210:211], off
	v_lshl_add_u64 v[212:213], s[46:47], 0, v[198:199]
	s_mov_b32 m0, s50
	s_addc_u32 s9, s47, 0
	global_load_lds_dwordx4 v[212:213], off
	v_lshl_add_u64 v[244:245], s[8:9], 0, v[196:197]
	s_mov_b32 m0, s51
	v_cndmask_b32_e64 v67, 0, 1, s[4:5]
	global_load_lds_dwordx4 v[244:245], off
	v_lshl_add_u64 v[244:245], s[8:9], 0, v[198:199]
	s_mov_b32 m0, s52
	v_cmp_ne_u32_e64 s[8:9], 1, v67
	global_load_lds_dwordx4 v[244:245], off
	s_mov_b32 m0, s31
	s_andn2_b64 vcc, exec, s[4:5]
	global_load_lds_dwordx4 v64, s[48:49] nt
	s_mov_b32 m0, s53
	s_nop 0
	global_load_lds_dwordx4 v66, s[48:49] nt
	s_waitcnt vmcnt(8)
	s_waitcnt lgkmcnt(0)
	s_barrier
	s_cbranch_vccnz .LBB0_1530
	s_setprio 1
	s_waitcnt lgkmcnt(0)
	v_mfma_f32_16x16x128_f8f6f4 v[128:131], v[16:23], v[56:63], v[128:131]
	v_mfma_f32_16x16x128_f8f6f4 v[120:123], v[24:31], v[56:63], v[120:123]
	v_mfma_f32_16x16x128_f8f6f4 v[112:115], v[16:23], v[48:55], v[112:115]
	v_mfma_f32_16x16x128_f8f6f4 v[104:107], v[24:31], v[48:55], v[104:107]
	v_mfma_f32_16x16x128_f8f6f4 v[96:99], v[16:23], v[40:47], v[96:99]
	v_mfma_f32_16x16x128_f8f6f4 v[88:91], v[24:31], v[40:47], v[88:91]
	v_mfma_f32_16x16x128_f8f6f4 v[80:83], v[16:23], v[32:39], v[80:83]
	v_mfma_f32_16x16x128_f8f6f4 v[72:75], v[24:31], v[32:39], v[72:75]
	s_setprio 0
	s_setprio 1
	v_mfma_f32_16x16x128_f8f6f4 v[124:127], v[0:7], v[56:63], v[124:127]
	v_mfma_f32_16x16x128_f8f6f4 v[116:119], v[8:15], v[56:63], v[116:119]
	v_mfma_f32_16x16x128_f8f6f4 v[108:111], v[0:7], v[48:55], v[108:111]
	v_mfma_f32_16x16x128_f8f6f4 v[100:103], v[8:15], v[48:55], v[100:103]
	v_mfma_f32_16x16x128_f8f6f4 v[92:95], v[0:7], v[40:47], v[92:95]
	v_mfma_f32_16x16x128_f8f6f4 v[84:87], v[8:15], v[40:47], v[84:87]
	v_mfma_f32_16x16x128_f8f6f4 v[76:79], v[0:7], v[32:39], v[76:79]
	v_mfma_f32_16x16x128_f8f6f4 v[68:71], v[8:15], v[32:39], v[68:71]
	s_setprio 0
; #define PG8_STAGE(bufoff, gbase, voff) do { _Pragma("unroll") for (int _i = 0; _i < 2; ++_i) \
;         __builtin_amdgcn_global_load_lds((const unsigned*)((const char*)(gbase) + (voff)[_i]), (PG8_LAS unsigned*)(lds + (bufoff) + ldsw + _i * 8192), 16, 0, 0); } while (0)
; #define PG8_WAIT_V(n) asm volatile("s_waitcnt vmcnt(" #n ")" ::: "memory")
; #define PG8_WAIT_L(n) asm volatile("s_waitcnt lgkmcnt(" #n ")" ::: "memory")
; #define PG8_BAR __builtin_amdgcn_s_barrier()
; #define PG8_SCHED __builtin_amdgcn_sched_barrier(0)
; template <class Epi, class Sched, bool ALIGN_EPI = false, bool SP2 = false>
; __device__ __forceinline__ void gemm_phase(PG8_LAS unsigned char* lds, const Geo geo, const Sched& S, const Epi& E, const int wave_) {
;     ...
;             PG8_LDB(B0, 1, 0); PG8_LDB(B1, 1, 1); PG8_SCHED; PG8_LDA(At, 1, 0); PG8_STAGE(PG8_SA(0, 1), a2 + hstepA, s1);
;             PG8_WAIT_V(8); PG8_WAIT_L(0); PG8_BAR; PG8_MMA(0, 0, At, B0); PG8_MMA(0, 1, At, B1); PG8_BAR; PG8_SCHED;
;             PG8_LDA(At, 1, 1); PG8_STAGE(PG8_SB(1, 0), b3, voffB); PG8_STAGE(PG8_SB(1, 1), b3 + hstepB, voffB); PG8_STAGE(PG8_SA(1, 0), a3, s0);
;             PG8_WAIT_V(8); PG8_WAIT_L(0); PG8_BAR; if (h1) { PG8_MMA(1, 0, At, B0); PG8_MMA(1, 1, At, B1); } PG8_BAR; PG8_SCHED;
.LBB0_1530:
	v_mov_b32_e32 v67, v65
	v_lshl_add_u64 v[244:245], s[48:49], 0, v[64:65]
	v_lshl_add_u64 v[66:67], s[48:49], 0, v[66:67]
	v_cndmask_b32_e64 v64, v202, v205, s[6:7]
	v_cndmask_b32_e64 v243, v204, v239, s[6:7]
	s_barrier
	ds_read_b128 v[16:19], v227
	ds_read_b128 v[20:23], v228
	ds_read_b128 v[24:27], v229
	ds_read_b128 v[28:31], v230
	ds_read_b128 v[0:3], v231
	ds_read_b128 v[4:7], v232
	ds_read_b128 v[8:11], v233
	ds_read_b128 v[12:15], v234
	s_mov_b32 m0, s54
	s_waitcnt lgkmcnt(0)
	ds_read_b128 v[32:35], v235 offset:32768
	ds_read_b128 v[36:39], v235 offset:33792
	ds_read_b128 v[40:43], v235 offset:34816
	ds_read_b128 v[44:47], v235 offset:35840
	ds_read_b128 v[48:51], v235 offset:36864
	ds_read_b128 v[52:55], v235 offset:37888
	ds_read_b128 v[56:59], v235 offset:38912
	ds_read_b128 v[60:63], v235 offset:39936
	global_load_lds_dwordx4 v64, s[48:49] nt
	s_mov_b32 m0, s55
	s_nop 0
	global_load_lds_dwordx4 v243, s[48:49] nt
	s_waitcnt vmcnt(8)
	s_waitcnt lgkmcnt(0)
	s_barrier
	s_setprio 1
	s_waitcnt lgkmcnt(0)
	v_mfma_f32_16x16x128_f8f6f4 v[192:195], v[16:23], v[32:39], v[192:195]
	v_mfma_f32_16x16x128_f8f6f4 v[184:187], v[24:31], v[32:39], v[184:187]
	v_mfma_f32_16x16x128_f8f6f4 v[176:179], v[16:23], v[40:47], v[176:179]
	v_mfma_f32_16x16x128_f8f6f4 v[168:171], v[24:31], v[40:47], v[168:171]
	v_mfma_f32_16x16x128_f8f6f4 v[160:163], v[16:23], v[48:55], v[160:163]
	v_mfma_f32_16x16x128_f8f6f4 v[152:155], v[24:31], v[48:55], v[152:155]
	v_mfma_f32_16x16x128_f8f6f4 v[144:147], v[16:23], v[56:63], v[144:147]
	v_mfma_f32_16x16x128_f8f6f4 v[136:139], v[24:31], v[56:63], v[136:139]
	s_setprio 0
	s_setprio 1
	v_mfma_f32_16x16x128_f8f6f4 v[188:191], v[0:7], v[32:39], v[188:191]
	v_mfma_f32_16x16x128_f8f6f4 v[180:183], v[8:15], v[32:39], v[180:183]
	v_mfma_f32_16x16x128_f8f6f4 v[172:175], v[0:7], v[40:47], v[172:175]
	v_mfma_f32_16x16x128_f8f6f4 v[164:167], v[8:15], v[40:47], v[164:167]
	v_mfma_f32_16x16x128_f8f6f4 v[156:159], v[0:7], v[48:55], v[156:159]
	v_mfma_f32_16x16x128_f8f6f4 v[148:151], v[8:15], v[48:55], v[148:151]
	v_mfma_f32_16x16x128_f8f6f4 v[140:143], v[0:7], v[56:63], v[140:143]
	v_mfma_f32_16x16x128_f8f6f4 v[132:135], v[8:15], v[56:63], v[132:135]
	s_setprio 0
	s_barrier
	s_mov_b32 m0, s70
	v_lshl_add_u64 v[210:211], v[210:211], 0, s[16:17]
	s_add_u32 s6, s46, 0x400080
	ds_read_b128 v[56:59], v235 offset:49152
	ds_read_b128 v[60:63], v235 offset:50176
	ds_read_b128 v[48:51], v235 offset:51200
	ds_read_b128 v[52:55], v235 offset:52224
	ds_read_b128 v[40:43], v235 offset:53248
	ds_read_b128 v[44:47], v235 offset:54272
	ds_read_b128 v[32:35], v235 offset:55296
	ds_read_b128 v[36:39], v235 offset:56320
	global_load_lds_dwordx4 v[210:211], off
	v_lshl_add_u64 v[210:211], v[212:213], 0, s[16:17]
	s_mov_b32 m0, s72
	s_addc_u32 s7, s47, 0
	global_load_lds_dwordx4 v[210:211], off
	v_lshl_add_u64 v[210:211], s[6:7], 0, v[196:197]
	s_mov_b32 m0, s95
	v_lshl_add_u64 v[66:67], v[66:67], 0, s[16:17]
	global_load_lds_dwordx4 v[210:211], off
	v_lshl_add_u64 v[210:211], s[6:7], 0, v[198:199]
	s_mov_b32 m0, s97
	s_and_b64 vcc, exec, s[8:9]
	global_load_lds_dwordx4 v[210:211], off
	v_lshl_add_u64 v[210:211], v[244:245], 0, s[16:17]
	s_mov_b32 m0, s74
	s_nop 0
	global_load_lds_dwordx4 v[210:211], off
	s_mov_b32 m0, s82
	s_nop 0
	global_load_lds_dwordx4 v[66:67], off
	s_waitcnt vmcnt(8)
	s_waitcnt lgkmcnt(0)
	s_barrier
	s_cbranch_vccnz .LBB0_1525
	s_setprio 1
	s_waitcnt lgkmcnt(0)
	v_mfma_f32_16x16x128_f8f6f4 v[128:131], v[16:23], v[56:63], v[128:131]
	v_mfma_f32_16x16x128_f8f6f4 v[120:123], v[24:31], v[56:63], v[120:123]
	v_mfma_f32_16x16x128_f8f6f4 v[112:115], v[16:23], v[48:55], v[112:115]
	v_mfma_f32_16x16x128_f8f6f4 v[104:107], v[24:31], v[48:55], v[104:107]
	v_mfma_f32_16x16x128_f8f6f4 v[96:99], v[16:23], v[40:47], v[96:99]
	v_mfma_f32_16x16x128_f8f6f4 v[88:91], v[24:31], v[40:47], v[88:91]
	v_mfma_f32_16x16x128_f8f6f4 v[80:83], v[16:23], v[32:39], v[80:83]
	v_mfma_f32_16x16x128_f8f6f4 v[72:75], v[24:31], v[32:39], v[72:75]
	s_setprio 0
	s_setprio 1
	v_mfma_f32_16x16x128_f8f6f4 v[124:127], v[0:7], v[56:63], v[124:127]
	v_mfma_f32_16x16x128_f8f6f4 v[116:119], v[8:15], v[56:63], v[116:119]
	v_mfma_f32_16x16x128_f8f6f4 v[108:111], v[0:7], v[48:55], v[108:111]
	v_mfma_f32_16x16x128_f8f6f4 v[100:103], v[8:15], v[48:55], v[100:103]
	v_mfma_f32_16x16x128_f8f6f4 v[92:95], v[0:7], v[40:47], v[92:95]
	v_mfma_f32_16x16x128_f8f6f4 v[84:87], v[8:15], v[40:47], v[84:87]
	v_mfma_f32_16x16x128_f8f6f4 v[76:79], v[0:7], v[32:39], v[76:79]
	v_mfma_f32_16x16x128_f8f6f4 v[68:71], v[8:15], v[32:39], v[68:71]
	s_setprio 0
	s_branch .LBB0_1525
